# speedup vs baseline: 1.0910x; 1.0014x over previous
.LBB3_4:
	s_or_b64 exec, exec, s[6:7]
	s_load_dwordx8 s[40:47], s[0:1], 0x28
	s_lshl_b32 s0, s12, 1
	v_lshlrev_b32_e32 v18, 4, v35
	s_mov_b32 s1, 0
	v_mov_b32_e32 v19, 0
	s_waitcnt lgkmcnt(0)
	v_lshl_add_u64 v[62:63], s[8:9], 0, v[18:19]
	s_lshl_b64 s[4:5], s[0:1], 10
	v_lshl_add_u64 v[64:65], s[10:11], 0, v[18:19]
	v_lshl_add_u64 v[18:19], v[62:63], 0, s[4:5]
	v_lshl_add_u64 v[84:85], v[62:63], 0, s[4:5]
	v_lshl_add_u64 v[86:87], v[64:65], 0, s[4:5]
	global_load_dwordx4 v[18:21], v[18:19], off
	v_lshl_add_u64 v[22:23], v[64:65], 0, s[4:5]
	global_load_dwordx4 v[54:57], v[22:23], off
	global_load_dwordx4 v[76:79], v[84:85], off offset:1024
	global_load_dwordx4 v[80:83], v[86:87], off offset:1024
	s_mov_b32 s4, 0x5040100
	s_waitcnt vmcnt(33)
	v_perm_b32 v22, v4, v2, s4
	v_cvt_f32_f16_e32 v4, v4
	s_waitcnt vmcnt(32)
	v_perm_b32 v58, v5, v3, s4
	v_cvt_f32_f16_e32 v5, v5
	s_waitcnt vmcnt(21)
	v_perm_b32 v25, v16, v14, s4
	v_mul_f32_e32 v4, v4, v4
	v_fma_mix_f32 v2, v2, v2, v4 op_sel_hi:[1,1,0]
	v_mul_f32_e32 v4, v5, v5
	v_fma_mix_f32 v3, v3, v3, v4 op_sel_hi:[1,1,0]
	v_fma_mix_f32 v2, v6, v6, v2 op_sel_hi:[1,1,0]
	v_fma_mix_f32 v3, v7, v7, v3 op_sel_hi:[1,1,0]
	v_fma_mix_f32 v2, v8, v8, v2 op_sel_hi:[1,1,0]
	v_fma_mix_f32 v3, v9, v9, v3 op_sel_hi:[1,1,0]
	v_fma_mix_f32 v2, v10, v10, v2 op_sel_hi:[1,1,0]
	v_fma_mix_f32 v3, v11, v11, v3 op_sel_hi:[1,1,0]
	v_fma_mix_f32 v2, v12, v12, v2 op_sel_hi:[1,1,0]
	v_fma_mix_f32 v3, v13, v13, v3 op_sel_hi:[1,1,0]
	v_perm_b32 v24, v12, v10, s4
	v_perm_b32 v23, v8, v6, s4
	v_fma_mix_f32 v2, v14, v14, v2 op_sel_hi:[1,1,0]
	v_fma_mix_f32 v3, v15, v15, v3 op_sel_hi:[1,1,0]
	s_waitcnt vmcnt(20)
	v_perm_b32 v61, v17, v15, s4
	v_perm_b32 v60, v13, v11, s4
	v_perm_b32 v59, v9, v7, s4
	v_fma_mix_f32 v70, v16, v16, v2 op_sel_hi:[1,1,0]
	v_fma_mix_f32 v71, v17, v17, v3 op_sel_hi:[1,1,0]
	s_or_b32 s0, s0, 1
	s_lshl_b64 s[0:1], s[0:1], 10
	s_waitcnt vmcnt(4)
	v_perm_b32 v69, v53, v51, s4
	v_perm_b32 v68, v49, v47, s4
	v_perm_b32 v67, v45, v43, s4
	v_perm_b32 v66, v41, v39, s4
	v_fma_mix_f32 v39, v39, v39, v71 op_sel_hi:[1,1,0]
	s_mulk_i32 s12, 0x1100
	v_fma_mix_f32 v39, v41, v41, v39 op_sel_hi:[1,1,0]
	s_waitcnt vmcnt(3)
	v_mfma_f32_32x32x16_f16 v[2:17], v[18:21], v[22:25], 0
	v_fma_mix_f32 v39, v43, v43, v39 op_sel_hi:[1,1,0]
	s_nop 0
	v_fma_mix_f32 v39, v45, v45, v39 op_sel_hi:[1,1,0]
	s_nop 0
	v_fma_mix_f32 v39, v47, v47, v39 op_sel_hi:[1,1,0]
	s_nop 0
	v_fma_mix_f32 v39, v49, v49, v39 op_sel_hi:[1,1,0]
	s_waitcnt vmcnt(2)
	v_mfma_f32_32x32x16_f16 v[2:17], v[54:57], v[22:25], v[2:17]
	v_mfma_f32_32x32x16_f16 v[18:33], v[18:21], v[58:61], 0
	v_mfma_f32_32x32x16_f16 v[18:33], v[54:57], v[58:61], v[18:33]
	v_perm_b32 v65, v52, v50, s4
	v_perm_b32 v64, v48, v46, s4
	v_perm_b32 v63, v44, v42, s4
	v_perm_b32 v62, v40, v38, s4
	v_fma_mix_f32 v38, v38, v38, v70 op_sel_hi:[1,1,0]
	v_cmp_gt_u32_e64 s[0:1], 32, v35
	v_fma_mix_f32 v38, v40, v40, v38 op_sel_hi:[1,1,0]
	v_fma_mix_f32 v40, v51, v51, v39 op_sel_hi:[1,1,0]
	v_fma_mix_f32 v38, v42, v42, v38 op_sel_hi:[1,1,0]
	s_waitcnt vmcnt(1)
	v_mfma_f32_32x32x16_f16 v[2:17], v[76:79], v[62:65], v[2:17]
	v_fma_mix_f32 v38, v44, v44, v38 op_sel_hi:[1,1,0]
	s_nop 0
	v_fma_mix_f32 v38, v46, v46, v38 op_sel_hi:[1,1,0]
	s_nop 0
	v_fma_mix_f32 v38, v48, v48, v38 op_sel_hi:[1,1,0]
	s_nop 0
	v_fma_mix_f32 v38, v50, v50, v38 op_sel_hi:[1,1,0]
	v_mfma_f32_32x32x16_f16 v[18:33], v[76:79], v[66:69], v[18:33]
	v_fma_mix_f32 v39, v52, v52, v38 op_sel_hi:[1,1,0]
	v_fma_mix_f32 v38, v53, v53, v40 op_sel_hi:[1,1,0]
	s_waitcnt vmcnt(0)
	v_mfma_f32_32x32x16_f16 v[2:17], v[80:83], v[62:65], v[2:17]
	v_mfma_f32_32x32x16_f16 v[18:33], v[80:83], v[66:69], v[18:33]
	s_nop 10
	v_mov_b32_e32 v10, v39
	v_mov_b32_e32 v11, v39
	v_mov_b32_e32 v12, v38
	v_mov_b32_e32 v13, v38
	v_permlane32_swap_b32_e32 v10, v11
	s_nop 0
	v_permlane32_swap_b32_e32 v12, v13
	s_and_saveexec_b64 s[4:5], s[0:1]
	s_cbranch_execz .LBB3_6
	v_and_b32_e32 v15, 32, v0
	v_cmp_eq_u32_e64 s[0:1], 0, v15
	v_lshl_add_u32 v14, v1, 2, s12
	s_nop 0
	v_cndmask_b32_e64 v10, v10, v11, s[0:1]
	v_cndmask_b32_e64 v11, v12, v13, s[0:1]
	v_add_f32_e32 v10, v39, v10
	v_add_f32_e32 v11, v38, v11
	ds_write2_b32 v14, v10, v11 offset1:32

	.amdhsa_kernel _Z5k3_vqPKDF16_S0_S0_S0_PKfPiPfS3_S4_
		.amdhsa_group_segment_fixed_size 56768
		.amdhsa_private_segment_fixed_size 0
		.amdhsa_kernarg_size 72
		.amdhsa_user_sgpr_count 2
		.amdhsa_user_sgpr_dispatch_ptr 0
		.amdhsa_user_sgpr_queue_ptr 0
		.amdhsa_user_sgpr_kernarg_segment_ptr 1
		.amdhsa_user_sgpr_dispatch_id 0
		.amdhsa_user_sgpr_kernarg_preload_length 0
		.amdhsa_user_sgpr_kernarg_preload_offset 0
		.amdhsa_user_sgpr_private_segment_size 0
		.amdhsa_uses_dynamic_stack 0
		.amdhsa_enable_private_segment 0
		.amdhsa_system_sgpr_workgroup_id_x 1
		.amdhsa_system_sgpr_workgroup_id_y 0
		.amdhsa_system_sgpr_workgroup_id_z 0
		.amdhsa_system_sgpr_workgroup_info 0
		.amdhsa_system_vgpr_workitem_id 0
		.amdhsa_next_free_vgpr 88
		.amdhsa_next_free_sgpr 91
		.amdhsa_accum_offset 88
		.amdhsa_reserve_vcc 1
		.amdhsa_float_round_mode_32 0
		.amdhsa_float_round_mode_16_64 0
		.amdhsa_float_denorm_mode_32 3
		.amdhsa_float_denorm_mode_16_64 3
		.amdhsa_dx10_clamp 1
		.amdhsa_ieee_mode 1
		.amdhsa_fp16_overflow 0
		.amdhsa_tg_split 0
		.amdhsa_exception_fp_ieee_invalid_op 0
		.amdhsa_exception_fp_denorm_src 0
		.amdhsa_exception_fp_ieee_div_zero 0
		.amdhsa_exception_fp_ieee_overflow 0
		.amdhsa_exception_fp_ieee_underflow 0
		.amdhsa_exception_fp_ieee_inexact 0
		.amdhsa_exception_int_div_zero 0
	.end_amdhsa_kernel

amdhsa.kernels:
  - .agpr_count:     0
    .args:
      - .offset:         0
        .size:           272
        .value_kind:     by_value
    .group_segment_fixed_size: 27780
    .kernarg_segment_align: 8
    .kernarg_segment_size: 272
    .language:       OpenCL C
    .language_version:
      - 2
      - 0
    .max_flat_workgroup_size: 1024
    .name:           _Z6k_prep5PrepP
    .private_segment_fixed_size: 0
    .sgpr_count:     106
    .sgpr_spill_count: 0
    .symbol:         _Z6k_prep5PrepP.kd
    .uniform_work_group_size: 1
    .uses_dynamic_stack: false
    .vgpr_count:     135
    .vgpr_spill_count: 0
    .wavefront_size: 64
  - .agpr_count:     0
    .args:
      - .actual_access:  read_only
        .address_space:  global
        .offset:         0
        .size:           8
        .value_kind:     global_buffer
      - .actual_access:  read_only
        .address_space:  global
        .offset:         8
        .size:           8
        .value_kind:     global_buffer
      - .actual_access:  read_only
        .address_space:  global
        .offset:         16
        .size:           8
        .value_kind:     global_buffer
      - .address_space:  global
        .offset:         24
        .size:           8
        .value_kind:     global_buffer
      - .actual_access:  read_only
        .address_space:  global
        .offset:         32
        .size:           8
        .value_kind:     global_buffer
      - .actual_access:  read_only
        .address_space:  global
        .offset:         40
        .size:           8
        .value_kind:     global_buffer
      - .actual_access:  read_only
        .address_space:  global
        .offset:         48
        .size:           8
        .value_kind:     global_buffer
      - .actual_access:  read_only
        .address_space:  global
        .offset:         56
        .size:           8
        .value_kind:     global_buffer
      - .actual_access:  write_only
        .address_space:  global
        .offset:         64
        .size:           8
        .value_kind:     global_buffer
    .group_segment_fixed_size: 0
    .kernarg_segment_align: 8
    .kernarg_segment_size: 72
    .language:       OpenCL C
    .language_version:
      - 2
      - 0
    .max_flat_workgroup_size: 384
    .name:           _Z11k1_temporalPKfS0_S0_PKDF16_S0_S0_S0_S0_Pf
    .private_segment_fixed_size: 0
    .sgpr_count:     34
    .sgpr_spill_count: 0
    .symbol:         _Z11k1_temporalPKfS0_S0_PKDF16_S0_S0_S0_S0_Pf.kd
    .uniform_work_group_size: 1
    .uses_dynamic_stack: false
    .vgpr_count:     247
    .vgpr_spill_count: 0
    .wavefront_size: 64
  - .agpr_count:     0
    .args:
      - .address_space:  global
        .offset:         0
        .size:           8
        .value_kind:     global_buffer
      - .address_space:  global
        .offset:         8
        .size:           8
        .value_kind:     global_buffer
      - .actual_access:  read_only
        .address_space:  global
        .offset:         16
        .size:           8
        .value_kind:     global_buffer
      - .actual_access:  read_only
        .address_space:  global
        .offset:         24
        .size:           8
        .value_kind:     global_buffer
      - .actual_access:  read_only
        .address_space:  global
        .offset:         32
        .size:           8
        .value_kind:     global_buffer
      - .actual_access:  read_only
        .address_space:  global
        .offset:         40
        .size:           8
        .value_kind:     global_buffer
      - .actual_access:  read_only
        .address_space:  global
        .offset:         48
        .size:           8
        .value_kind:     global_buffer
      - .actual_access:  read_only
        .address_space:  global
        .offset:         56
        .size:           8
        .value_kind:     global_buffer
      - .actual_access:  read_only
        .address_space:  global
        .offset:         64
        .size:           8
        .value_kind:     global_buffer
      - .actual_access:  read_only
        .address_space:  global
        .offset:         72
        .size:           8
        .value_kind:     global_buffer
      - .actual_access:  read_only
        .address_space:  global
        .offset:         80
        .size:           8
        .value_kind:     global_buffer
      - .actual_access:  read_only
        .address_space:  global
        .offset:         88
        .size:           8
        .value_kind:     global_buffer
      - .actual_access:  read_only
        .address_space:  global
        .offset:         96
        .size:           8
        .value_kind:     global_buffer
      - .actual_access:  read_only
        .address_space:  global
        .offset:         104
        .size:           8
        .value_kind:     global_buffer
      - .actual_access:  read_only
        .address_space:  global
        .offset:         112
        .size:           8
        .value_kind:     global_buffer
      - .actual_access:  read_only
        .address_space:  global
        .offset:         120
        .size:           8
        .value_kind:     global_buffer
      - .address_space:  global
        .offset:         128
        .size:           8
        .value_kind:     global_buffer
      - .actual_access:  write_only
        .address_space:  global
        .offset:         136
        .size:           8
        .value_kind:     global_buffer
      - .actual_access:  write_only
        .address_space:  global
        .offset:         144
        .size:           8
        .value_kind:     global_buffer
      - .actual_access:  write_only
        .address_space:  global
        .offset:         152
        .size:           8
        .value_kind:     global_buffer
      - .actual_access:  write_only
        .address_space:  global
        .offset:         160
        .size:           8
        .value_kind:     global_buffer
    .group_segment_fixed_size: 0
    .kernarg_segment_align: 8
    .kernarg_segment_size: 168
    .language:       OpenCL C
    .language_version:
      - 2
      - 0
    .max_flat_workgroup_size: 512
    .name:           _Z10k2_featurePKfPKDF16_S0_S0_S0_S0_S0_S0_PKyS0_S0_S0_S0_S0_S0_S0_PfS5_S5_S5_S5_
    .private_segment_fixed_size: 0
    .sgpr_count:     38
    .sgpr_spill_count: 0
    .symbol:         _Z10k2_featurePKfPKDF16_S0_S0_S0_S0_S0_S0_PKyS0_S0_S0_S0_S0_S0_S0_PfS5_S5_S5_S5_.kd
    .uniform_work_group_size: 1
    .uses_dynamic_stack: false
    .vgpr_count:     256
    .vgpr_spill_count: 0
    .wavefront_size: 64
  - .agpr_count:     0
    .args:
      - .actual_access:  read_only
        .address_space:  global
        .offset:         0
        .size:           8
        .value_kind:     global_buffer
      - .actual_access:  read_only
        .address_space:  global
        .offset:         8
        .size:           8
        .value_kind:     global_buffer
      - .actual_access:  read_only
        .address_space:  global
        .offset:         16
        .size:           8
        .value_kind:     global_buffer
      - .actual_access:  read_only
        .address_space:  global
        .offset:         24
        .size:           8
        .value_kind:     global_buffer
      - .actual_access:  read_only
        .address_space:  global
        .offset:         32
        .size:           8
        .value_kind:     global_buffer
      - .actual_access:  write_only
        .address_space:  global
        .offset:         40
        .size:           8
        .value_kind:     global_buffer
      - .actual_access:  write_only
        .address_space:  global
        .offset:         48
        .size:           8
        .value_kind:     global_buffer
      - .address_space:  global
        .offset:         56
        .size:           8
        .value_kind:     global_buffer
      - .actual_access:  write_only
        .address_space:  global
        .offset:         64
        .size:           8
        .value_kind:     global_buffer
    .group_segment_fixed_size: 56768
    .kernarg_segment_align: 8
    .kernarg_segment_size: 72
    .language:       OpenCL C
    .language_version:
      - 2
      - 0
    .max_flat_workgroup_size: 768
    .name:           _Z5k3_vqPKDF16_S0_S0_S0_PKfPiPfS3_S4_
    .private_segment_fixed_size: 0
    .sgpr_count:     54
    .sgpr_spill_count: 0
    .symbol:         _Z5k3_vqPKDF16_S0_S0_S0_PKfPiPfS3_S4_.kd
    .uniform_work_group_size: 1
    .uses_dynamic_stack: false
    .vgpr_count:     88
    .vgpr_spill_count: 0
    .wavefront_size: 64
  - .agpr_count:     0
    .args:
      - .actual_access:  read_only
        .address_space:  global
        .offset:         0
        .size:           8
        .value_kind:     global_buffer
      - .actual_access:  read_only
        .address_space:  global
        .offset:         8
        .size:           8
        .value_kind:     global_buffer
      - .address_space:  global
        .offset:         16
        .size:           8
        .value_kind:     global_buffer
      - .actual_access:  read_only
        .address_space:  global
        .offset:         24
        .size:           8
        .value_kind:     global_buffer
      - .actual_access:  read_only
        .address_space:  global
        .offset:         32
        .size:           8
        .value_kind:     global_buffer
      - .actual_access:  read_only
        .address_space:  global
        .offset:         40
        .size:           8
        .value_kind:     global_buffer
      - .actual_access:  read_only
        .address_space:  global
        .offset:         48
        .size:           8
        .value_kind:     global_buffer
      - .actual_access:  read_only
        .address_space:  global
        .offset:         56
        .size:           8
        .value_kind:     global_buffer
      - .actual_access:  read_only
        .address_space:  global
        .offset:         64
        .size:           8
        .value_kind:     global_buffer
      - .actual_access:  read_only
        .address_space:  global
        .offset:         72
        .size:           8
        .value_kind:     global_buffer
      - .actual_access:  read_only
        .address_space:  global
        .offset:         80
        .size:           8
        .value_kind:     global_buffer
      - .address_space:  global
        .offset:         88
        .size:           8
        .value_kind:     global_buffer
      - .actual_access:  read_only
        .address_space:  global
        .offset:         96
        .size:           8
        .value_kind:     global_buffer
      - .actual_access:  read_only
        .address_space:  global
        .offset:         104
        .size:           8
        .value_kind:     global_buffer
      - .actual_access:  read_only
        .address_space:  global
        .offset:         112
        .size:           8
        .value_kind:     global_buffer
      - .actual_access:  read_only
        .address_space:  global
        .offset:         120
        .size:           8
        .value_kind:     global_buffer
      - .actual_access:  read_only
        .address_space:  global
        .offset:         128
        .size:           8
        .value_kind:     global_buffer
      - .address_space:  global
        .offset:         136
        .size:           8
        .value_kind:     global_buffer
      - .address_space:  global
        .offset:         144
        .size:           8
        .value_kind:     global_buffer
      - .actual_access:  write_only
        .address_space:  global
        .offset:         152
        .size:           8
        .value_kind:     global_buffer
      - .offset:         160
        .size:           4
        .value_kind:     hidden_block_count_x
      - .offset:         164
        .size:           4
        .value_kind:     hidden_block_count_y
      - .offset:         168
        .size:           4
        .value_kind:     hidden_block_count_z
      - .offset:         172
        .size:           2
        .value_kind:     hidden_group_size_x
      - .offset:         174
        .size:           2
        .value_kind:     hidden_group_size_y
      - .offset:         176
        .size:           2
        .value_kind:     hidden_group_size_z
      - .offset:         178
        .size:           2
        .value_kind:     hidden_remainder_x
      - .offset:         180
        .size:           2
        .value_kind:     hidden_remainder_y
      - .offset:         182
        .size:           2
        .value_kind:     hidden_remainder_z
      - .offset:         200
        .size:           8
        .value_kind:     hidden_global_offset_x
      - .offset:         208
        .size:           8
        .value_kind:     hidden_global_offset_y
      - .offset:         216
        .size:           8
        .value_kind:     hidden_global_offset_z
      - .offset:         224
        .size:           2
        .value_kind:     hidden_grid_dims
      - .offset:         280
        .size:           4
        .value_kind:     hidden_dynamic_lds_size
    .group_segment_fixed_size: 0
    .kernarg_segment_align: 8
    .kernarg_segment_size: 416
    .language:       OpenCL C
    .language_version:
      - 2
      - 0
    .max_flat_workgroup_size: 768
    .name:           _Z7k5_convPKDF16_PKiS0_PKfS4_S4_S4_S4_S4_S4_S4_PfS4_S4_S2_S2_S4_PiS5_S5_
    .private_segment_fixed_size: 0
    .sgpr_count:     54
    .sgpr_spill_count: 0
    .symbol:         _Z7k5_convPKDF16_PKiS0_PKfS4_S4_S4_S4_S4_S4_S4_PfS4_S4_S2_S2_S4_PiS5_S5_.kd
    .uniform_work_group_size: 1
    .uses_dynamic_stack: false
    .vgpr_count:     88
    .vgpr_spill_count: 0
    .wavefront_size: 64
